# c45: c41 + FINAL phase row-norm wave reductions via DPP/permlane-swap adds (no LDS bpermute round trips)
# baseline (speedup 1.0000x reference)
; #define GAS __attribute__((address_space(1)))
; __device__ __forceinline__ float wave_sum(float v) {
; #pragma unroll
;     for (int o = 1; o < 64; o <<= 1) v += __shfl_xor(v, o);
;     return v;
; }
; __global__ void __launch_bounds__(NTHREADS, 2) fwd(Args args) {
;     ...
;                 float s = 0.f;
; #pragma unroll
;                 for (int q = 0; q < 4; ++q) s += (v[q].x * v[q].x + v[q].y * v[q].y) + (v[q].z * v[q].z + v[q].w * v[q].w);
;                 const float rstd = 1.0f / sqrtf(wave_sum(s) * (1.0f / DM) + RMS_EPS);
;                 GAS f32x4* xr = (GAS f32x4*)(H + (size_t)t * DM) + F.lane;
; #pragma unroll
;                 for (int q = 0; q < 4; ++q) __builtin_nontemporal_store(v[q] * rstd * gn[q], xr + 64 * q); }
.LBB0_1478:
	v_pk_mul_f32 v[16:17], v[32:33], v[32:33]
	v_pk_mul_f32 v[18:19], v[34:35], v[34:35]
	s_addk_i32 s25, 0x1000
	v_pk_mov_b32 v[20:21], v[18:19], v[16:17] op_sel:[1,0]
	v_mov_b32_e32 v19, v17
	v_pk_add_f32 v[16:17], v[20:21], v[18:19]
	v_pk_mul_f32 v[18:19], v[36:37], v[36:37]
	v_pk_mul_f32 v[20:21], v[38:39], v[38:39]
	v_pk_add_f32 v[16:17], v[16:17], v[16:17] op_sel:[0,1] op_sel_hi:[1,0]
	v_pk_mov_b32 v[22:23], v[20:21], v[18:19] op_sel:[1,0]
	v_mov_b32_e32 v21, v19
	v_pk_add_f32 v[18:19], v[22:23], v[20:21]
	v_mul_f32_e32 v20, v46, v46
	v_mul_f32_e32 v21, v47, v47
	v_pk_add_f32 v[18:19], v[18:19], v[18:19] op_sel:[0,1] op_sel_hi:[1,0]
	v_mov_b32_e32 v17, v20
	v_mov_b32_e32 v19, v21
	v_pk_add_f32 v[16:17], v[16:17], v[18:19]
	v_mul_f32_e32 v18, v43, v43
	v_mul_f32_e32 v20, v41, v41
	v_mul_f32_e32 v22, v44, v44
	v_mul_f32_e32 v23, v45, v45
	v_pk_fma_f32 v[18:19], v[42:43], v[42:43], v[18:19] op_sel_hi:[1,1,0]
	v_pk_fma_f32 v[20:21], v[40:41], v[40:41], v[20:21] op_sel_hi:[1,1,0]
	v_mov_b32_e32 v19, v22
	v_mov_b32_e32 v21, v23
	v_pk_add_f32 v[18:19], v[18:19], v[20:21]
	s_addk_i32 s4, 0x2000
	v_pk_add_f32 v[16:17], v[16:17], v[18:19]
	s_cmpk_lt_i32 s25, 0x3000
	v_add_f32_e32 v16, v16, v17
	v_lshl_add_u64 v[58:59], v[58:59], 0, s[10:11]
	s_waitcnt lgkmcnt(0)
	s_nop 1
	v_add_f32_dpp v16, v16, v16 quad_perm:[1,0,3,2] row_mask:0xf bank_mask:0xf
	s_waitcnt lgkmcnt(0)
	s_nop 1
	v_add_f32_dpp v16, v16, v16 quad_perm:[2,3,0,1] row_mask:0xf bank_mask:0xf
	s_waitcnt lgkmcnt(0)
	s_nop 1
	v_add_f32_dpp v16, v16, v16 row_half_mirror row_mask:0xf bank_mask:0xf
	s_waitcnt lgkmcnt(0)
	s_nop 1
	v_add_f32_dpp v16, v16, v16 row_mirror row_mask:0xf bank_mask:0xf
	s_waitcnt lgkmcnt(0)
	v_mov_b32_e32 v17, v16
	s_nop 1
	v_permlane16_swap_b32_e32 v16, v17
	v_add_f32_e32 v16, v16, v17
	s_waitcnt lgkmcnt(0)
	v_mov_b32_e32 v17, v16
	s_nop 1
	v_permlane32_swap_b32_e32 v16, v17
	v_add_f32_e32 v16, v16, v17
	v_fmamk_f32 v16, v16, 0x3a800000, v82
	v_mul_f32_e32 v17, 0x4f800000, v16
	v_cmp_gt_f32_e32 vcc, s33, v16
	s_nop 1
	v_cndmask_b32_e32 v16, v16, v17, vcc
	v_sqrt_f32_e32 v17, v16
	s_nop 0
	v_add_u32_e32 v18, -1, v17
	v_add_u32_e32 v19, 1, v17
	v_fma_f32 v20, -v18, v17, v16
	v_fma_f32 v21, -v19, v17, v16
	v_cmp_ge_f32_e64 s[0:1], 0, v20
	s_nop 1
	v_cndmask_b32_e64 v17, v17, v18, s[0:1]
	v_cmp_lt_f32_e64 s[0:1], 0, v21
	s_nop 1
	v_cndmask_b32_e64 v17, v17, v19, s[0:1]
	v_mul_f32_e32 v18, 0x37800000, v17
	v_cndmask_b32_e32 v17, v17, v18, vcc
	v_cmp_class_f32_e32 vcc, v16, v83
	s_nop 1
	v_cndmask_b32_e32 v16, v17, v16, vcc
	v_div_scale_f32 v17, s[0:1], v16, v16, 1.0
	v_rcp_f32_e32 v18, v17
	v_div_scale_f32 v19, vcc, 1.0, v16, 1.0
	v_fma_f32 v20, -v17, v18, 1.0
	v_fmac_f32_e32 v18, v20, v18
	v_mul_f32_e32 v20, v19, v18
	v_fma_f32 v21, -v17, v20, v19
	v_fmac_f32_e32 v20, v21, v18
	v_fma_f32 v17, -v17, v20, v19
	v_div_fmas_f32 v17, v17, v18, v20
	v_div_fixup_f32 v20, v17, v16, 1.0
	v_pk_mul_f32 v[16:17], v[20:21], v[34:35] op_sel_hi:[0,1]
	v_pk_mul_f32 v[18:19], v[20:21], v[32:33] op_sel_hi:[0,1]
	v_pk_mul_f32 v[18:19], v[18:19], v[2:3]
	v_pk_mul_f32 v[16:17], v[16:17], v[0:1]
	global_store_dwordx4 v[56:57], v[16:19], off nt
	s_nop 1
	v_pk_mul_f32 v[16:17], v[20:21], v[38:39] op_sel_hi:[0,1]
	v_pk_mul_f32 v[18:19], v[20:21], v[36:37] op_sel_hi:[0,1]
	v_pk_mul_f32 v[18:19], v[18:19], v[6:7]
	v_pk_mul_f32 v[16:17], v[16:17], v[4:5]
	global_store_dwordx4 v[56:57], v[16:19], off offset:1024 nt
	s_nop 1
	v_pk_mul_f32 v[16:17], v[20:21], v[42:43] op_sel_hi:[0,1]
	v_pk_mul_f32 v[18:19], v[20:21], v[40:41] op_sel_hi:[0,1]
	v_pk_mul_f32 v[18:19], v[18:19], v[10:11]
	v_pk_mul_f32 v[16:17], v[16:17], v[8:9]
	global_store_dwordx4 v[56:57], v[16:19], off offset:2048 nt
	s_nop 1
	v_pk_mul_f32 v[16:17], v[20:21], v[46:47] op_sel_hi:[0,1]
	v_pk_mul_f32 v[18:19], v[20:21], v[44:45] op_sel_hi:[0,1]
	v_pk_mul_f32 v[18:19], v[18:19], v[14:15]
	v_pk_mul_f32 v[16:17], v[16:17], v[12:13]
	global_store_dwordx4 v[56:57], v[16:19], off offset:3072 nt
	v_lshl_add_u64 v[56:57], v[56:57], 0, s[8:9]
	s_cbranch_scc0 .LBB0_1495

; #define GAS __attribute__((address_space(1)))
; __device__ __forceinline__ float wave_sum(float v) {
; #pragma unroll
;     for (int o = 1; o < 64; o <<= 1) v += __shfl_xor(v, o);
;     return v;
; }
; __global__ void __launch_bounds__(NTHREADS, 2) fwd(Args args) {
;     ...
;                 float s = 0.f;
; #pragma unroll
;                 for (int q = 0; q < 4; ++q) s += (v[q].x * v[q].x + v[q].y * v[q].y) + (v[q].z * v[q].z + v[q].w * v[q].w);
;                 const float rstd = 1.0f / sqrtf(wave_sum(s) * (1.0f / DM) + RMS_EPS);
;                 GAS f32x4* xr = (GAS f32x4*)(H + (size_t)t * DM) + F.lane;
; #pragma unroll
;                 for (int q = 0; q < 4; ++q) __builtin_nontemporal_store(v[q] * rstd * gn[q], xr + 64 * q); }
.LBB0_1487:
	v_pk_mul_f32 v[16:17], v[32:33], v[32:33]
	v_pk_mul_f32 v[18:19], v[34:35], v[34:35]
	v_lshlrev_b32_e32 v68, 16, v66
	v_pk_mov_b32 v[20:21], v[18:19], v[16:17] op_sel:[1,0]
	v_mov_b32_e32 v19, v17
	v_pk_add_f32 v[16:17], v[20:21], v[18:19]
	v_pk_mul_f32 v[18:19], v[36:37], v[36:37]
	v_pk_mul_f32 v[20:21], v[38:39], v[38:39]
	v_pk_add_f32 v[16:17], v[16:17], v[16:17] op_sel:[0,1] op_sel_hi:[1,0]
	v_pk_mov_b32 v[22:23], v[20:21], v[18:19] op_sel:[1,0]
	v_mov_b32_e32 v21, v19
	v_pk_add_f32 v[18:19], v[22:23], v[20:21]
	v_mul_f32_e32 v20, v46, v46
	v_mul_f32_e32 v21, v47, v47
	v_pk_add_f32 v[18:19], v[18:19], v[18:19] op_sel:[0,1] op_sel_hi:[1,0]
	v_mov_b32_e32 v17, v20
	v_mov_b32_e32 v19, v21
	v_pk_add_f32 v[16:17], v[16:17], v[18:19]
	v_mul_f32_e32 v18, v43, v43
	v_mul_f32_e32 v20, v41, v41
	v_mul_f32_e32 v22, v44, v44
	v_mul_f32_e32 v23, v45, v45
	v_pk_fma_f32 v[18:19], v[42:43], v[42:43], v[18:19] op_sel_hi:[1,1,0]
	v_pk_fma_f32 v[20:21], v[40:41], v[40:41], v[20:21] op_sel_hi:[1,1,0]
	v_mov_b32_e32 v19, v22
	v_mov_b32_e32 v21, v23
	v_pk_add_f32 v[18:19], v[18:19], v[20:21]
	v_and_b32_e32 v69, 0xffff0000, v66
	v_pk_add_f32 v[16:17], v[16:17], v[18:19]
	v_lshlrev_b32_e32 v70, 16, v64
	v_add_f32_e32 v16, v16, v17
	v_and_b32_e32 v71, 0xffff0000, v64
	s_ashr_i32 s5, s35, 8
	v_lshlrev_b32_e32 v48, 16, v60
	v_and_b32_e32 v49, 0xffff0000, v60
	s_waitcnt lgkmcnt(0)
	s_nop 1
	v_add_f32_dpp v16, v16, v16 quad_perm:[1,0,3,2] row_mask:0xf bank_mask:0xf
	v_and_b32_e32 v51, 0xffff0000, v61
	s_cmpk_lt_i32 s5, 0x80
	s_waitcnt lgkmcnt(0)
	s_nop 1
	v_add_f32_dpp v16, v16, v16 quad_perm:[2,3,0,1] row_mask:0xf bank_mask:0xf
	s_waitcnt lgkmcnt(0)
	s_nop 1
	v_add_f32_dpp v16, v16, v16 row_half_mirror row_mask:0xf bank_mask:0xf
	s_waitcnt lgkmcnt(0)
	s_nop 1
	v_add_f32_dpp v16, v16, v16 row_mirror row_mask:0xf bank_mask:0xf
	s_waitcnt lgkmcnt(0)
	v_mov_b32_e32 v17, v16
	s_nop 1
	v_permlane16_swap_b32_e32 v16, v17
	v_add_f32_e32 v16, v16, v17
	s_waitcnt lgkmcnt(0)
	v_mov_b32_e32 v17, v16
	s_nop 1
	v_permlane32_swap_b32_e32 v16, v17
	v_add_f32_e32 v16, v16, v17
	v_fmamk_f32 v16, v16, 0x3a800000, v82
	v_mul_f32_e32 v17, 0x4f800000, v16
	v_cmp_gt_f32_e32 vcc, s33, v16
	s_nop 1
	v_cndmask_b32_e32 v16, v16, v17, vcc
	v_sqrt_f32_e32 v17, v16
	s_nop 0
	v_add_u32_e32 v18, -1, v17
	v_add_u32_e32 v19, 1, v17
	v_fma_f32 v20, -v18, v17, v16
	v_fma_f32 v21, -v19, v17, v16
	v_cmp_ge_f32_e64 s[0:1], 0, v20
	s_nop 1
	v_cndmask_b32_e64 v17, v17, v18, s[0:1]
	v_cmp_lt_f32_e64 s[0:1], 0, v21
	s_nop 1
	v_cndmask_b32_e64 v17, v17, v19, s[0:1]
	v_mul_f32_e32 v18, 0x37800000, v17
	v_cndmask_b32_e32 v17, v17, v18, vcc
	v_cmp_class_f32_e32 vcc, v16, v83
	s_nop 1
	v_cndmask_b32_e32 v16, v17, v16, vcc
	v_div_scale_f32 v17, s[0:1], v16, v16, 1.0
	v_rcp_f32_e32 v18, v17
	v_div_scale_f32 v19, vcc, 1.0, v16, 1.0
	s_mov_b64 s[0:1], -1
	v_fma_f32 v20, -v17, v18, 1.0
	v_fmac_f32_e32 v18, v20, v18
	v_mul_f32_e32 v20, v19, v18
	v_fma_f32 v21, -v17, v20, v19
	v_fmac_f32_e32 v20, v21, v18
	v_fma_f32 v17, -v17, v20, v19
	v_div_fmas_f32 v17, v17, v18, v20
	v_div_fixup_f32 v20, v17, v16, 1.0
	v_pk_mul_f32 v[16:17], v[20:21], v[34:35] op_sel_hi:[0,1]
	v_pk_mul_f32 v[18:19], v[20:21], v[32:33] op_sel_hi:[0,1]
	v_pk_mul_f32 v[18:19], v[18:19], v[2:3]
	v_pk_mul_f32 v[16:17], v[16:17], v[0:1]
	global_store_dwordx4 v[56:57], v[16:19], off offset:-4096 nt
	s_nop 1
	v_pk_mul_f32 v[16:17], v[20:21], v[38:39] op_sel_hi:[0,1]
	v_pk_mul_f32 v[18:19], v[20:21], v[36:37] op_sel_hi:[0,1]
	v_pk_mul_f32 v[18:19], v[18:19], v[6:7]
	v_pk_mul_f32 v[16:17], v[16:17], v[4:5]
	global_store_dwordx4 v[56:57], v[16:19], off offset:-3072 nt
	s_nop 1
	v_pk_mul_f32 v[16:17], v[20:21], v[42:43] op_sel_hi:[0,1]
	v_pk_mul_f32 v[18:19], v[20:21], v[40:41] op_sel_hi:[0,1]
	v_pk_mul_f32 v[18:19], v[18:19], v[10:11]
	v_pk_mul_f32 v[16:17], v[16:17], v[8:9]
	global_store_dwordx4 v[56:57], v[16:19], off offset:-2048 nt
	s_nop 1
	v_pk_mul_f32 v[16:17], v[20:21], v[46:47] op_sel_hi:[0,1]
	v_pk_mul_f32 v[18:19], v[20:21], v[44:45] op_sel_hi:[0,1]
	v_pk_mul_f32 v[18:19], v[18:19], v[14:15]
	v_pk_mul_f32 v[16:17], v[16:17], v[12:13]
	global_store_dwordx4 v[56:57], v[16:19], off offset:-1024 nt
	v_lshlrev_b32_e32 v44, 16, v62
	v_and_b32_e32 v45, 0xffff0000, v62
	v_alignbit_b32 v16, v67, v66, 16
	v_and_b32_e32 v66, 0xffff0000, v16
	v_alignbit_b32 v16, v65, v64, 16
	v_and_b32_e32 v64, 0xffff0000, v16
	v_alignbit_b32 v16, v63, v62, 16
	v_and_b32_e32 v46, 0xffff0000, v16
	v_alignbit_b32 v16, v61, v60, 16
	v_and_b32_e32 v67, 0xffff0000, v67
	v_and_b32_e32 v65, 0xffff0000, v65
	v_and_b32_e32 v47, 0xffff0000, v63
	v_and_b32_e32 v50, 0xffff0000, v16
	s_cbranch_scc1 .LBB0_1489
; #define GAS __attribute__((address_space(1)))
; __global__ void __launch_bounds__(NTHREADS, 2) fwd(Args args) {
;     ...
;                     } else { const int lt = (slot >> 8) - 128, rl = slot & 255; const float gt = GATES[2 * t + k] * (1.0f / 32.0f);
; #pragma unroll
;                         for (int q = 0; q < 4; ++q) { const GAS f32x4* pp = (const GAS f32x4*)(PART + (size_t)((lt * 4 + q) * 7) * 65536 + rl * 256) + F.lane; f32x4 s = pp[0];
; #pragma unroll
;                             for (int s7 = 1; s7 < 7; ++s7) s += pp[(size_t)s7 * 16384];
	s_add_u32 s14, s21, s14
	s_addc_u32 s15, s22, s15
	s_lshl_b32 s0, s35, 10
	s_and_b32 s0, s0, 0x3fc00
	s_add_u32 s0, s23, s0
	s_mul_i32 s5, s5, 28
	s_addc_u32 s1, s24, 0
	s_add_i32 s2, s5, 0xfffff200
	s_lshl_b64 s[16:17], s[2:3], 18
	s_add_u32 s16, s0, s16
	s_addc_u32 s17, s1, s17
	v_lshl_add_u64 v[36:37], s[16:17], 0, v[52:53]
	v_add_co_u32_e32 v28, vcc, s26, v36
	s_add_i32 s2, s5, 0xfffff207
	s_nop 0
	v_addc_co_u32_e32 v29, vcc, 0, v37, vcc
	v_add_co_u32_e32 v30, vcc, s27, v36
	global_load_dword v163, v53, s[14:15]
	global_load_dwordx4 v[16:19], v52, s[16:17]
	v_addc_co_u32_e32 v31, vcc, 0, v37, vcc
	v_add_co_u32_e32 v38, vcc, s28, v36
	s_lshl_b64 s[14:15], s[2:3], 18
	s_nop 0
	v_addc_co_u32_e32 v39, vcc, 0, v37, vcc
	v_add_co_u32_e32 v40, vcc, s29, v36
	s_add_u32 s14, s0, s14
	s_nop 0
	v_addc_co_u32_e32 v41, vcc, 0, v37, vcc
	v_add_co_u32_e32 v60, vcc, s30, v36
	s_addc_u32 s15, s1, s15
	s_nop 0
	v_addc_co_u32_e32 v61, vcc, 0, v37, vcc
	v_add_co_u32_e32 v62, vcc, s31, v36
	v_lshl_add_u64 v[100:101], s[14:15], 0, v[52:53]
	s_nop 0
	v_addc_co_u32_e32 v63, vcc, 0, v37, vcc
	v_add_co_u32_e32 v92, vcc, s26, v100
	s_add_i32 s2, s5, 0xfffff20e
	s_nop 0
	v_addc_co_u32_e32 v93, vcc, 0, v101, vcc
	v_add_co_u32_e32 v94, vcc, s27, v100
	s_lshl_b64 s[16:17], s[2:3], 18
	s_nop 0
	v_addc_co_u32_e32 v95, vcc, 0, v101, vcc
	v_add_co_u32_e32 v102, vcc, s28, v100
	s_add_u32 s16, s0, s16
	s_nop 0
	v_addc_co_u32_e32 v103, vcc, 0, v101, vcc
	v_add_co_u32_e32 v104, vcc, s29, v100
	s_addc_u32 s17, s1, s17
	s_nop 0
	v_addc_co_u32_e32 v105, vcc, 0, v101, vcc
	v_add_co_u32_e32 v108, vcc, s30, v100
	v_lshl_add_u64 v[132:133], s[16:17], 0, v[52:53]
	s_nop 0
	v_addc_co_u32_e32 v109, vcc, 0, v101, vcc
	v_add_co_u32_e32 v110, vcc, s31, v100
	s_add_i32 s2, s5, 0xfffff215
	s_nop 0
	v_addc_co_u32_e32 v111, vcc, 0, v101, vcc
	v_add_co_u32_e32 v116, vcc, s26, v132
	global_load_dwordx4 v[20:23], v[28:29], off
	global_load_dwordx4 v[24:27], v[30:31], off
	v_addc_co_u32_e32 v117, vcc, 0, v133, vcc
	v_add_co_u32_e32 v120, vcc, s27, v132
	global_load_dwordx4 v[28:31], v[38:39], off
	global_load_dwordx4 v[32:35], v[40:41], off
	v_addc_co_u32_e32 v121, vcc, 0, v133, vcc
	v_add_co_u32_e32 v124, vcc, s28, v132
	global_load_dwordx4 v[36:39], v[60:61], off
	global_load_dwordx4 v[40:43], v[62:63], off
	v_addc_co_u32_e32 v125, vcc, 0, v133, vcc
	v_add_co_u32_e32 v128, vcc, s29, v132
	global_load_dwordx4 v[60:63], v[92:93], off
	global_load_dwordx4 v[72:75], v[94:95], off
	v_addc_co_u32_e32 v129, vcc, 0, v133, vcc
	global_load_dwordx4 v[92:95], v[102:103], off
	global_load_dwordx4 v[96:99], v[104:105], off
	s_nop 0
	global_load_dwordx4 v[100:103], v[108:109], off
	global_load_dwordx4 v[104:107], v[110:111], off
	s_nop 0
	global_load_dwordx4 v[108:111], v52, s[14:15]
	global_load_dwordx4 v[112:115], v52, s[16:17]
	v_add_co_u32_e32 v134, vcc, s30, v132
	s_lshl_b64 s[14:15], s[2:3], 18
	s_nop 0
	v_addc_co_u32_e32 v135, vcc, 0, v133, vcc
	s_add_u32 s0, s0, s14
	v_add_co_u32_e32 v136, vcc, s31, v132
	s_addc_u32 s1, s1, s15
	s_nop 0
	v_addc_co_u32_e32 v137, vcc, 0, v133, vcc
	v_lshl_add_u64 v[160:161], s[0:1], 0, v[52:53]
	v_add_co_u32_e32 v144, vcc, s26, v160
	global_load_dwordx4 v[116:119], v[116:117], off
	s_nop 0
	global_load_dwordx4 v[120:123], v[120:121], off
	v_addc_co_u32_e32 v145, vcc, 0, v161, vcc
	v_add_co_u32_e32 v148, vcc, s27, v160
	global_load_dwordx4 v[124:127], v[124:125], off
	s_nop 0
	global_load_dwordx4 v[128:131], v[128:129], off
	v_addc_co_u32_e32 v149, vcc, 0, v161, vcc
	v_add_co_u32_e32 v152, vcc, s28, v160
	global_load_dwordx4 v[132:135], v[134:135], off
	s_nop 0
	global_load_dwordx4 v[136:139], v[136:137], off
	v_addc_co_u32_e32 v153, vcc, 0, v161, vcc
	v_add_co_u32_e32 v156, vcc, s29, v160
	global_load_dwordx4 v[140:143], v52, s[0:1]
	s_nop 0
	v_addc_co_u32_e32 v157, vcc, 0, v161, vcc
	global_load_dwordx4 v[144:147], v[144:145], off
	s_nop 0
	global_load_dwordx4 v[148:151], v[148:149], off
	v_add_co_u32_e32 v164, vcc, s30, v160
	global_load_dwordx4 v[152:155], v[152:153], off
	s_nop 0
	global_load_dwordx4 v[156:159], v[156:157], off
	v_addc_co_u32_e32 v165, vcc, 0, v161, vcc
	v_add_co_u32_e32 v160, vcc, 0x180000, v160
	global_load_dwordx4 v[164:167], v[164:165], off
	s_nop 0
	v_addc_co_u32_e32 v161, vcc, 0, v161, vcc
	global_load_dwordx4 v[168:171], v[160:161], off
	s_waitcnt vmcnt(28)
; #define GAS __attribute__((address_space(1)))
; __global__ void __launch_bounds__(NTHREADS, 2) fwd(Args args) {
;     ...
;                     } else { const int lt = (slot >> 8) - 128, rl = slot & 255; const float gt = GATES[2 * t + k] * (1.0f / 32.0f);
; #pragma unroll
;                         for (int q = 0; q < 4; ++q) { const GAS f32x4* pp = (const GAS f32x4*)(PART + (size_t)((lt * 4 + q) * 7) * 65536 + rl * 256) + F.lane; f32x4 s = pp[0];
; #pragma unroll
;                             for (int s7 = 1; s7 < 7; ++s7) s += pp[(size_t)s7 * 16384];
;                             v[q] += s * gt; } } }
	v_mul_f32_e32 v160, 0x3d000000, v163
	s_waitcnt vmcnt(26)
	v_pk_add_f32 v[18:19], v[18:19], v[22:23]
	v_pk_add_f32 v[16:17], v[16:17], v[20:21]
	s_waitcnt vmcnt(25)
	v_pk_add_f32 v[18:19], v[18:19], v[26:27]
	v_pk_add_f32 v[16:17], v[16:17], v[24:25]
	s_waitcnt vmcnt(24)
	v_pk_add_f32 v[18:19], v[18:19], v[30:31]
	v_pk_add_f32 v[16:17], v[16:17], v[28:29]
	s_waitcnt vmcnt(23)
	v_pk_add_f32 v[18:19], v[18:19], v[34:35]
	v_pk_add_f32 v[16:17], v[16:17], v[32:33]
	s_waitcnt vmcnt(22)
	v_pk_add_f32 v[18:19], v[18:19], v[38:39]
	v_pk_add_f32 v[16:17], v[16:17], v[36:37]
	s_waitcnt vmcnt(21)
	v_pk_add_f32 v[18:19], v[18:19], v[42:43]
	v_pk_add_f32 v[16:17], v[16:17], v[40:41]
	v_pk_fma_f32 v[18:19], v[160:161], v[18:19], v[66:67] op_sel_hi:[0,1,1]
	v_pk_fma_f32 v[16:17], v[160:161], v[16:17], v[68:69] op_sel_hi:[0,1,1]
	s_waitcnt vmcnt(14)
	v_pk_add_f32 v[20:21], v[110:111], v[62:63]
	v_pk_add_f32 v[22:23], v[108:109], v[60:61]
	v_pk_add_f32 v[20:21], v[20:21], v[74:75]
	v_pk_add_f32 v[22:23], v[22:23], v[72:73]
	v_pk_add_f32 v[20:21], v[20:21], v[94:95]
	v_pk_add_f32 v[22:23], v[22:23], v[92:93]
	v_pk_add_f32 v[20:21], v[20:21], v[98:99]
	v_pk_add_f32 v[22:23], v[22:23], v[96:97]
	v_pk_add_f32 v[20:21], v[20:21], v[102:103]
	v_pk_add_f32 v[22:23], v[22:23], v[100:101]
	v_pk_add_f32 v[20:21], v[20:21], v[106:107]
	v_pk_add_f32 v[24:25], v[22:23], v[104:105]
	v_pk_fma_f32 v[22:23], v[160:161], v[20:21], v[64:65] op_sel_hi:[0,1,1]
	v_pk_fma_f32 v[20:21], v[160:161], v[24:25], v[70:71] op_sel_hi:[0,1,1]
	s_waitcnt vmcnt(12)
	v_pk_add_f32 v[24:25], v[114:115], v[118:119]
	v_pk_add_f32 v[26:27], v[112:113], v[116:117]
	s_waitcnt vmcnt(11)
	v_pk_add_f32 v[24:25], v[24:25], v[122:123]
	v_pk_add_f32 v[26:27], v[26:27], v[120:121]
	s_waitcnt vmcnt(10)
	v_pk_add_f32 v[24:25], v[24:25], v[126:127]
	v_pk_add_f32 v[26:27], v[26:27], v[124:125]
	s_waitcnt vmcnt(9)
	v_pk_add_f32 v[24:25], v[24:25], v[130:131]
	v_pk_add_f32 v[26:27], v[26:27], v[128:129]
	s_waitcnt vmcnt(8)
	v_pk_add_f32 v[24:25], v[24:25], v[134:135]
	v_pk_add_f32 v[26:27], v[26:27], v[132:133]
	s_waitcnt vmcnt(7)
	v_pk_add_f32 v[24:25], v[24:25], v[138:139]
	v_pk_add_f32 v[28:29], v[26:27], v[136:137]
	v_pk_fma_f32 v[26:27], v[160:161], v[24:25], v[46:47] op_sel_hi:[0,1,1]
	v_pk_fma_f32 v[24:25], v[160:161], v[28:29], v[44:45] op_sel_hi:[0,1,1]
	s_waitcnt vmcnt(5)
	v_pk_add_f32 v[28:29], v[142:143], v[146:147]
	v_pk_add_f32 v[30:31], v[140:141], v[144:145]
	s_waitcnt vmcnt(4)
	v_pk_add_f32 v[28:29], v[28:29], v[150:151]
	v_pk_add_f32 v[30:31], v[30:31], v[148:149]
	s_waitcnt vmcnt(3)
	v_pk_add_f32 v[28:29], v[28:29], v[154:155]
	v_pk_add_f32 v[30:31], v[30:31], v[152:153]
	s_waitcnt vmcnt(2)
	v_pk_add_f32 v[28:29], v[28:29], v[158:159]
	v_pk_add_f32 v[30:31], v[30:31], v[156:157]
	s_waitcnt vmcnt(1)
	v_pk_add_f32 v[28:29], v[28:29], v[166:167]
	v_pk_add_f32 v[30:31], v[30:31], v[164:165]
	s_waitcnt vmcnt(0)
	v_pk_add_f32 v[28:29], v[28:29], v[170:171]
	v_pk_add_f32 v[32:33], v[30:31], v[168:169]
	v_pk_fma_f32 v[30:31], v[160:161], v[28:29], v[50:51] op_sel_hi:[0,1,1]
	v_pk_fma_f32 v[28:29], v[160:161], v[32:33], v[48:49] op_sel_hi:[0,1,1]
	s_cbranch_execnz .LBB0_1491
	s_branch .LBB0_1490
